# phase 3: cumulative-sum items remapped so the four items on one XCD share a batch element (strided forget-gate lines fetched once per XCD L2), on top of the row-norm rebalance
# baseline (speedup 1.0000x reference)
.LBB0_556:
	s_or_b64 exec, exec, s[6:7]
	s_cmp_gt_i32 s2, 31
	s_cbranch_scc1 .LBB0_571
	v_mbcnt_lo_u32_b32 v0, -1, 0
	v_mbcnt_hi_u32_b32 v2, -1, v0
	v_and_b32_e32 v3, 64, v2
	v_add_u32_e32 v4, -1, v2
	v_cmp_lt_i32_e32 vcc, v4, v3
	s_load_dwordx2 s[26:27], s[0:1], 0x38
	v_mov_b32_e32 v147, 0
	v_cndmask_b32_e32 v4, v4, v2, vcc
	s_waitcnt vmcnt(0)
	v_lshlrev_b32_e32 v9, 2, v4
	v_add_u32_e32 v4, -2, v2
	v_cmp_lt_i32_e32 vcc, v4, v3
	s_mov_b64 s[20:21], 0x29d38000
	v_cmp_eq_u32_e64 s[4:5], 63, v217
	v_cndmask_b32_e32 v4, v4, v2, vcc
	v_lshlrev_b32_e32 v10, 2, v4
	v_add_u32_e32 v4, -4, v2
	v_cmp_lt_i32_e32 vcc, v4, v3
	s_mov_b32 s25, 0
	v_lshl_add_u32 v0, v1, 2, 0
	v_cndmask_b32_e32 v4, v4, v2, vcc
	v_lshlrev_b32_e32 v11, 2, v4
	v_add_u32_e32 v4, -8, v2
	v_cmp_lt_i32_e32 vcc, v4, v3
	v_cmp_lt_u32_e64 s[6:7], 63, v250
	v_cmp_eq_u32_e64 s[8:9], 0, v217
	v_cndmask_b32_e32 v4, v4, v2, vcc
	v_lshlrev_b32_e32 v12, 2, v4
	v_add_u32_e32 v4, -16, v2
	v_cmp_lt_i32_e32 vcc, v4, v3
	v_cmp_gt_u32_e64 s[10:11], 2, v217
	v_cmp_gt_u32_e64 s[12:13], 4, v217
	v_cndmask_b32_e32 v4, v4, v2, vcc
	v_lshlrev_b32_e32 v13, 2, v4
	v_subrev_u32_e32 v4, 32, v2
	v_cmp_lt_i32_e32 vcc, v4, v3
	v_cmp_gt_u32_e64 s[14:15], 8, v217
	v_cmp_gt_u32_e64 s[16:17], 16, v217
	v_cndmask_b32_e32 v2, v4, v2, vcc
	v_lshlrev_b32_e32 v14, 2, v2
	v_lshl_add_u64 v[2:3], s[76:77], 0, v[146:147]
	v_add_u32_e32 v4, -1, v1
	v_cmp_gt_u32_e64 s[18:19], 32, v217
	v_lshl_add_u64 v[2:3], v[2:3], 0, s[20:21]
	v_cmp_lt_u32_e64 s[20:21], 6, v4
	v_cmp_ne_u32_e64 s[22:23], 0, v1
	s_mov_b64 s[28:29], 0x20338140
	s_mov_b32 s3, 0xbfb8aa3b
	s_mov_b32 s40, 0x3f2aaaab
	v_mov_b32_e32 v15, 0x3ecc95a3
	s_mov_b32 s41, 0x3f317218
	s_mov_b32 s42, 0x7f800000
	v_mov_b32_e32 v16, 0x7f800000
	v_mov_b32_e32 v17, 0x7fc00000
	v_mov_b32_e32 v18, 0xff800000
	s_mov_b32 s43, 0x33800000
	s_mov_b32 s30, s2
	s_cmp_eq_u32 s80, 0x100
	s_cbranch_scc0 .Lp3c_keep
	s_and_b32 s98, s2, 7
	s_lshr_b32 s99, s98, 1
	s_lshl_b32 s99, s99, 3
	s_and_b32 s98, s98, 1
	s_lshl_b32 s98, s98, 2
	s_add_u32 s99, s99, s98
	s_lshr_b32 s98, s2, 3
	s_add_u32 s30, s99, s98
.Lp3c_keep:
	s_branch .LBB0_560
.LBB0_558:
	s_or_b64 exec, exec, s[36:37]
